# att9: K read addresses and slot rotation ahead of the tile barriers, rescale compare ahead of last block-1 MFMA
# speedup vs baseline: 1.0052x; 1.0052x over previous
; __device__ __forceinline__ void qkt64c(f32x16& p0, f32x16& p1, const char* Ks, const bf16x8* qr, const f32x16& cinit, int r32, int hi) {
; #pragma unroll
;     for (int d0 = 0; d0 < 4; ++d0) { const int cb = (d0 * 16 + hi * 8) * 2;
;         const bf16x8 b0 = *reinterpret_cast<const bf16x8*>(Ks + kswz<64>(r32, cb));
;         const bf16x8 b1 = *reinterpret_cast<const bf16x8*>(Ks + kswz<64>(32 + r32, cb));
;         if (d0 == 0) { p0 = __builtin_amdgcn_mfma_f32_32x32x16_bf16(b0, qr[0], cinit, 0, 0, 0); p1 = __builtin_amdgcn_mfma_f32_32x32x16_bf16(b1, qr[0], cinit, 0, 0, 0); }
;         else { p0 = __builtin_amdgcn_mfma_f32_32x32x16_bf16(b0, qr[d0], p0, 0, 0, 0); p1 = __builtin_amdgcn_mfma_f32_32x32x16_bf16(b1, qr[d0], p1, 0, 0, 0); } }
; }
.LBB0_823:
	s_lshl_b32 s2, s42, 13
	s_add_i32 s2, s2, 0
	v_add_u32_e32 v128, s2, v223
	v_add_u32_e32 v129, s2, v226
	v_add_u32_e32 v130, s2, v228
	v_add_u32_e32 v131, s2, v229
.Latt9_p1_top:
	ds_read_b128 v[144:147], v128 offset:49152
	ds_read_b128 v[148:151], v129 offset:49152
	ds_read_b128 v[152:155], v130 offset:49152
	ds_read_b128 v[156:159], v131 offset:49152
	ds_read_b128 v[232:235], v128 offset:53248
	ds_read_b128 v[236:239], v129 offset:53248
	ds_read_b128 v[240:243], v130 offset:53248
	ds_read_b128 v[244:247], v131 offset:53248
	v_lshl_add_u64 v[202:203], v[200:201], 0, s[64:65]
	s_mov_b32 s2, 0x8a40000
	v_add_co_u32_e32 v64, vcc, s2, v202
	s_mov_b32 s2, 0x8a50000
	s_nop 0
	v_addc_co_u32_e32 v65, vcc, 0, v203, vcc
	v_add_co_u32_e32 v66, vcc, s2, v202
	v_lshl_add_u64 v[204:205], v[198:199], 0, s[64:65]
	s_nop 0
	v_addc_co_u32_e32 v67, vcc, 0, v203, vcc
	s_mov_b32 s2, 0x6a40000
	global_load_dwordx4 v[178:181], v[64:65], off
	global_load_dwordx4 v[182:185], v[66:67], off
	v_add_co_u32_e32 v64, vcc, s2, v204
	s_nop 1
	v_addc_co_u32_e32 v65, vcc, 0, v205, vcc
	global_load_dwordx4 v[186:189], v[64:65], off
	v_exp_f32_e32 v190, v120
	v_exp_f32_e32 v191, v121
	v_add_f32_e32 v120, v96, v97
	v_add_f32_e32 v121, v98, v99
	s_waitcnt lgkmcnt(7)
	v_mfma_f32_32x32x16_bf16 v[128:143], v[144:147], v[162:165], v[80:95]
	v_exp_f32_e32 v192, v122
	v_add_f32_e32 v120, v120, v121
	v_add_f32_e32 v121, v100, v101
	v_add_f32_e32 v122, v102, v103
	v_exp_f32_e32 v193, v123
	s_waitcnt lgkmcnt(6)
	v_mfma_f32_32x32x16_bf16 v[128:143], v[148:151], v[166:169], v[128:143]
	v_add_f32_e32 v121, v121, v122
	v_add_f32_e32 v122, v104, v105
	v_add_f32_e32 v123, v106, v107
	v_add_f32_e32 v122, v122, v123
	v_add_f32_e32 v123, v108, v109
	s_waitcnt lgkmcnt(5)
	v_mfma_f32_32x32x16_bf16 v[128:143], v[152:155], v[170:173], v[128:143]
	v_add_f32_e32 v208, v110, v111
	v_add_f32_e32 v123, v123, v208
	v_add_f32_e32 v208, v112, v113
	v_add_f32_e32 v209, v114, v115
	v_add_f32_e32 v208, v208, v209
	s_waitcnt lgkmcnt(4)
	v_mfma_f32_32x32x16_bf16 v[128:143], v[156:159], v[174:177], v[128:143]
	v_exp_f32_e32 v124, v124
	v_exp_f32_e32 v125, v125
	s_waitcnt lgkmcnt(3)
	v_mfma_f32_32x32x16_bf16 v[144:159], v[232:235], v[162:165], v[80:95]
	v_lshl_add_u32 v234, s12, 14, v217
	ds_read_b64_tr_b16 v[64:65], v234 offset:0
	ds_read_b64_tr_b16 v[66:67], v234 offset:0x800
	ds_read_b64_tr_b16 v[68:69], v234 offset:0x1000
	ds_read_b64_tr_b16 v[70:71], v234 offset:0x1800
	ds_read_b64_tr_b16 v[72:73], v234 offset:0x2000
	ds_read_b64_tr_b16 v[74:75], v234 offset:0x2800
	ds_read_b64_tr_b16 v[76:77], v234 offset:0x3000
	ds_read_b64_tr_b16 v[78:79], v234 offset:0x3800
	v_exp_f32_e32 v126, v126
	v_exp_f32_e32 v127, v127
	v_add_f32_e32 v120, v208, v120
	v_add_f32_e32 v208, v116, v117
	v_add_f32_e32 v209, v118, v119
	v_add_f32_e32 v208, v208, v209
	v_add_f32_e32 v121, v208, v121
	s_waitcnt lgkmcnt(10)
	v_mfma_f32_32x32x16_bf16 v[144:159], v[236:239], v[166:169], v[144:159]
	v_add_f32_e32 v208, v190, v191
	v_add_f32_e32 v209, v192, v193
	v_add_f32_e32 v208, v208, v209
	v_add_f32_e32 v122, v122, v208
	v_add_f32_e32 v208, v124, v125
	v_add_f32_e32 v209, v126, v127
	v_add_f32_e32 v208, v208, v209
	s_waitcnt lgkmcnt(9)
	v_mfma_f32_32x32x16_bf16 v[144:159], v[240:243], v[170:173], v[144:159]
	v_add_f32_e32 v123, v123, v208
	v_add_f32_e32 v120, v120, v121
	v_add_f32_e32 v121, v122, v123
	v_add_f32_e32 v231, v120, v121
	v_mov_b32_e32 v232, v231
	v_cvt_pk_bf16_f32 v96, v96, v97
	v_cvt_pk_bf16_f32 v97, v98, v99
	s_waitcnt lgkmcnt(8)
	v_mfma_f32_32x32x16_bf16 v[144:159], v[244:247], v[174:177], v[144:159]
	v_cvt_pk_bf16_f32 v98, v100, v101
	v_cvt_pk_bf16_f32 v99, v102, v103
	v_cvt_pk_bf16_f32 v120, v104, v105
	v_cvt_pk_bf16_f32 v121, v106, v107
	v_cvt_pk_bf16_f32 v122, v108, v109
	v_cvt_pk_bf16_f32 v123, v110, v111
	v_permlane32_swap_b32_e32 v96, v98
	v_permlane32_swap_b32_e32 v97, v99
	v_cvt_pk_bf16_f32 v104, v112, v113
	v_cvt_pk_bf16_f32 v105, v114, v115
	v_cvt_pk_bf16_f32 v106, v116, v117
	v_cvt_pk_bf16_f32 v107, v118, v119
	s_waitcnt lgkmcnt(0)
	v_mfma_f32_32x32x16_bf16 v[0:15], v[96:99], v[64:67], v[0:15]
	v_permlane32_swap_b32_e32 v120, v122
	v_permlane32_swap_b32_e32 v121, v123
	v_cvt_pk_bf16_f32 v100, v190, v191
	v_cvt_pk_bf16_f32 v101, v192, v193
	v_cvt_pk_bf16_f32 v102, v124, v125
	v_cvt_pk_bf16_f32 v103, v126, v127
	v_mfma_f32_32x32x16_bf16 v[0:15], v[120:123], v[68:71], v[0:15]
	v_permlane32_swap_b32_e32 v104, v106
	v_permlane32_swap_b32_e32 v105, v107
	ds_read_b64_tr_b16 v[236:237], v234 offset:0x200
	ds_read_b64_tr_b16 v[238:239], v234 offset:0xa00
	ds_read_b64_tr_b16 v[240:241], v234 offset:0x1200
	ds_read_b64_tr_b16 v[242:243], v234 offset:0x1a00
	ds_read_b64_tr_b16 v[244:245], v234 offset:0x2200
	ds_read_b64_tr_b16 v[246:247], v234 offset:0x2a00
	ds_read_b64_tr_b16 v[190:191], v234 offset:0x3200
	ds_read_b64_tr_b16 v[192:193], v234 offset:0x3a00
	v_mfma_f32_32x32x16_bf16 v[0:15], v[104:107], v[72:75], v[0:15]
	v_permlane32_swap_b32_e32 v100, v102
	v_permlane32_swap_b32_e32 v101, v103
	v_permlane32_swap_b32_e32 v231, v232
	v_max_f32_e32 v108, v128, v129
	v_max3_f32 v109, v130, v131, v145
	v_max3_f32 v108, v108, v144, v146
	v_max3_f32 v108, v108, v147, v132
	v_max3_f32 v109, v109, v134, v135
	v_mfma_f32_32x32x16_bf16 v[0:15], v[100:103], v[76:79], v[0:15]
	v_max3_f32 v208, v108, v133, v148
	v_max3_f32 v209, v109, v150, v151
	ds_read_b64_tr_b16 v[124:125], v234 offset:0x400
	ds_read_b64_tr_b16 v[126:127], v234 offset:0xc00
	ds_read_b64_tr_b16 v[116:117], v234 offset:0x1400
	ds_read_b64_tr_b16 v[118:119], v234 offset:0x1c00
	ds_read_b64_tr_b16 v[112:113], v234 offset:0x2400
	ds_read_b64_tr_b16 v[114:115], v234 offset:0x2c00
	ds_read_b64_tr_b16 v[108:109], v234 offset:0x3400
	ds_read_b64_tr_b16 v[110:111], v234 offset:0x3c00
	s_waitcnt lgkmcnt(8)
	v_mfma_f32_32x32x16_bf16 v[48:63], v[96:99], v[236:239], v[48:63]
	v_max3_f32 v208, v208, v149, v136
	v_max3_f32 v209, v209, v138, v139
	v_max3_f32 v208, v208, v137, v152
	v_max3_f32 v209, v209, v154, v155
	v_max3_f32 v208, v208, v153, v140
	v_max3_f32 v209, v209, v142, v143
	v_max3_f32 v208, v208, v141, v156
	v_mfma_f32_32x32x16_bf16 v[48:63], v[120:123], v[240:243], v[48:63]
	v_max3_f32 v209, v209, v158, v159
	v_max3_f32 v208, v208, v157, v209
	v_mov_b32_e32 v209, v208
	s_nop 1
	v_permlane32_swap_b32_e32 v208, v209
	v_mfma_f32_32x32x16_bf16 v[48:63], v[104:107], v[244:247], v[48:63]
	v_max_f32_e32 v233, v208, v209
	s_mov_b32 s2, 0x4138aa3b
	v_cmp_ge_f32_e32 vcc, s2, v233
	v_mfma_f32_32x32x16_bf16 v[48:63], v[100:103], v[190:193], v[48:63]
	s_cmp_eq_u64 vcc, exec
	s_cbranch_scc0 .LBB0_836
	v_mov_b32_e32 v233, 1.0

; __device__ __forceinline__ void qkt64c(f32x16& p0, f32x16& p1, const char* Ks, const bf16x8* qr, const f32x16& cinit, int r32, int hi) {
; #pragma unroll
;     for (int d0 = 0; d0 < 4; ++d0) { const int cb = (d0 * 16 + hi * 8) * 2;
;         const bf16x8 b0 = *reinterpret_cast<const bf16x8*>(Ks + kswz<64>(r32, cb));
;         const bf16x8 b1 = *reinterpret_cast<const bf16x8*>(Ks + kswz<64>(32 + r32, cb));
;         if (d0 == 0) { p0 = __builtin_amdgcn_mfma_f32_32x32x16_bf16(b0, qr[0], cinit, 0, 0, 0); p1 = __builtin_amdgcn_mfma_f32_32x32x16_bf16(b1, qr[0], cinit, 0, 0, 0); }
;         else { p0 = __builtin_amdgcn_mfma_f32_32x32x16_bf16(b0, qr[d0], p0, 0, 0, 0); p1 = __builtin_amdgcn_mfma_f32_32x32x16_bf16(b1, qr[d0], p1, 0, 0, 0); } }
; }
.LBB0_829:
	v_add_co_u32_e32 v96, vcc, 0x8a60000, v202
	s_waitcnt lgkmcnt(0)
	s_nop 0
	v_addc_co_u32_e32 v97, vcc, 0, v203, vcc
	v_add_co_u32_e32 v98, vcc, 0x8a70000, v202
	s_nop 1
	v_addc_co_u32_e32 v99, vcc, 0, v203, vcc
	v_add_co_u32_e32 v100, vcc, 0x6a60000, v204
	s_nop 1
	v_addc_co_u32_e32 v101, vcc, 0, v205, vcc
	v_add_u32_e32 v102, s2, v223
	v_add_u32_e32 v103, s2, v226
	v_add_u32_e32 v104, s2, v228
	v_add_u32_e32 v105, s2, v229
	s_barrier
	ds_read_b128 v[112:115], v102 offset:49152
	ds_read_b128 v[116:119], v103 offset:49152
	ds_read_b128 v[120:123], v104 offset:49152
	ds_read_b128 v[124:127], v105 offset:49152
	ds_read_b128 v[190:193], v102 offset:53248
	ds_read_b128 v[202:205], v103 offset:53248
	ds_read_b128 v[234:237], v104 offset:53248
	ds_read_b128 v[238:241], v105 offset:53248
	global_load_dwordx4 v[178:181], v[96:97], off
	global_load_dwordx4 v[182:185], v[98:99], off
	global_load_dwordx4 v[186:189], v[100:101], off
	v_exp_f32_e32 v208, v152
	v_exp_f32_e32 v209, v153
	v_add_f32_e32 v152, v128, v129
	v_add_f32_e32 v153, v130, v131
	s_waitcnt lgkmcnt(7)
	v_mfma_f32_32x32x16_bf16 v[96:111], v[112:115], v[162:165], v[80:95]
	v_exp_f32_e32 v210, v154
	v_add_f32_e32 v152, v152, v153
	v_add_f32_e32 v153, v132, v133
	v_add_f32_e32 v154, v134, v135
	v_exp_f32_e32 v211, v155
	s_waitcnt lgkmcnt(6)
	v_mfma_f32_32x32x16_bf16 v[96:111], v[116:119], v[166:169], v[96:111]
	v_add_f32_e32 v153, v153, v154
	v_add_f32_e32 v154, v136, v137
	v_add_f32_e32 v155, v138, v139
	v_add_f32_e32 v154, v154, v155
	v_add_f32_e32 v155, v140, v141
	s_waitcnt lgkmcnt(5)
	v_mfma_f32_32x32x16_bf16 v[96:111], v[120:123], v[170:173], v[96:111]
	v_exp_f32_e32 v156, v156
	v_exp_f32_e32 v157, v157
	v_exp_f32_e32 v158, v158
	v_exp_f32_e32 v159, v159
	s_waitcnt lgkmcnt(4)
	v_mfma_f32_32x32x16_bf16 v[96:111], v[124:127], v[174:177], v[96:111]
	s_waitcnt lgkmcnt(3)
	v_mfma_f32_32x32x16_bf16 v[112:127], v[190:193], v[162:165], v[80:95]
	v_add_f32_e32 v190, v142, v143
	v_add_f32_e32 v155, v155, v190
	v_add_f32_e32 v190, v144, v145
	v_add_f32_e32 v191, v146, v147
	v_add_f32_e32 v190, v190, v191
	v_add_f32_e32 v152, v152, v190
	v_add_f32_e32 v190, v148, v149
	s_waitcnt lgkmcnt(2)
	v_mfma_f32_32x32x16_bf16 v[112:127], v[202:205], v[166:169], v[112:127]
	v_lshl_add_u32 v205, s42, 14, v217
	ds_read_b64_tr_b16 v[64:65], v205 offset:0
	ds_read_b64_tr_b16 v[66:67], v205 offset:0x800
	ds_read_b64_tr_b16 v[68:69], v205 offset:0x1000
	ds_read_b64_tr_b16 v[70:71], v205 offset:0x1800
	ds_read_b64_tr_b16 v[72:73], v205 offset:0x2000
	ds_read_b64_tr_b16 v[74:75], v205 offset:0x2800
	ds_read_b64_tr_b16 v[76:77], v205 offset:0x3000
	ds_read_b64_tr_b16 v[78:79], v205 offset:0x3800
	v_add_f32_e32 v191, v150, v151
	v_add_f32_e32 v190, v190, v191
	v_add_f32_e32 v153, v153, v190
	v_add_f32_e32 v190, v208, v209
	v_add_f32_e32 v191, v210, v211
	v_add_f32_e32 v190, v190, v191
	v_add_f32_e32 v154, v154, v190
	s_waitcnt lgkmcnt(9)
	v_mfma_f32_32x32x16_bf16 v[112:127], v[234:237], v[170:173], v[112:127]
	v_add_f32_e32 v190, v156, v157
	v_add_f32_e32 v191, v158, v159
	v_add_f32_e32 v190, v190, v191
	v_add_f32_e32 v155, v155, v190
	v_add_f32_e32 v152, v152, v153
	v_add_f32_e32 v153, v154, v155
	v_add_f32_e32 v203, v152, v153
	s_waitcnt lgkmcnt(8)
	v_mfma_f32_32x32x16_bf16 v[112:127], v[238:241], v[174:177], v[112:127]
	v_mov_b32_e32 v204, v203
	v_cvt_pk_bf16_f32 v152, v128, v129
	v_cvt_pk_bf16_f32 v153, v130, v131
	v_cvt_pk_bf16_f32 v154, v132, v133
	v_cvt_pk_bf16_f32 v155, v134, v135
	v_cvt_pk_bf16_f32 v136, v136, v137
	v_cvt_pk_bf16_f32 v137, v138, v139
	v_cvt_pk_bf16_f32 v138, v140, v141
	v_cvt_pk_bf16_f32 v139, v142, v143
	v_permlane32_swap_b32_e32 v152, v154
	v_permlane32_swap_b32_e32 v153, v155
	v_cvt_pk_bf16_f32 v132, v144, v145
	v_cvt_pk_bf16_f32 v133, v146, v147
	v_cvt_pk_bf16_f32 v134, v148, v149
	v_cvt_pk_bf16_f32 v135, v150, v151
	s_waitcnt lgkmcnt(0)
	v_mfma_f32_32x32x16_bf16 v[0:15], v[152:155], v[64:67], v[0:15]
	v_permlane32_swap_b32_e32 v136, v138
	v_permlane32_swap_b32_e32 v137, v139
	v_cvt_pk_bf16_f32 v128, v208, v209
	v_cvt_pk_bf16_f32 v129, v210, v211
	v_cvt_pk_bf16_f32 v130, v156, v157
	v_cvt_pk_bf16_f32 v131, v158, v159
	v_mfma_f32_32x32x16_bf16 v[0:15], v[136:139], v[68:71], v[0:15]
	v_permlane32_swap_b32_e32 v132, v134
	v_permlane32_swap_b32_e32 v133, v135
	ds_read_b64_tr_b16 v[190:191], v205 offset:0x200
	ds_read_b64_tr_b16 v[192:193], v205 offset:0xa00
	ds_read_b64_tr_b16 v[234:235], v205 offset:0x1200
	ds_read_b64_tr_b16 v[236:237], v205 offset:0x1a00
	ds_read_b64_tr_b16 v[238:239], v205 offset:0x2200
	ds_read_b64_tr_b16 v[240:241], v205 offset:0x2a00
	ds_read_b64_tr_b16 v[242:243], v205 offset:0x3200
	ds_read_b64_tr_b16 v[244:245], v205 offset:0x3a00
	v_mfma_f32_32x32x16_bf16 v[0:15], v[132:135], v[72:75], v[0:15]
	v_permlane32_swap_b32_e32 v128, v130
	v_permlane32_swap_b32_e32 v129, v131
	v_permlane32_swap_b32_e32 v203, v204
	v_max_f32_e32 v140, v96, v97
	v_max3_f32 v140, v140, v112, v114
	v_max3_f32 v141, v98, v99, v113
	v_max3_f32 v140, v140, v115, v100
	v_max3_f32 v141, v141, v102, v103
	v_mfma_f32_32x32x16_bf16 v[0:15], v[128:131], v[76:79], v[0:15]
	v_max3_f32 v202, v140, v101, v116
	v_max3_f32 v208, v141, v118, v119
	ds_read_b64_tr_b16 v[156:157], v205 offset:0x400
	ds_read_b64_tr_b16 v[158:159], v205 offset:0xc00
	ds_read_b64_tr_b16 v[148:149], v205 offset:0x1400
	ds_read_b64_tr_b16 v[150:151], v205 offset:0x1c00
	ds_read_b64_tr_b16 v[144:145], v205 offset:0x2400
	ds_read_b64_tr_b16 v[146:147], v205 offset:0x2c00
	ds_read_b64_tr_b16 v[140:141], v205 offset:0x3400
	ds_read_b64_tr_b16 v[142:143], v205 offset:0x3c00
	s_waitcnt lgkmcnt(8)
	v_mfma_f32_32x32x16_bf16 v[48:63], v[152:155], v[190:193], v[48:63]
	v_max3_f32 v190, v202, v117, v104
	v_max3_f32 v191, v208, v106, v107
	v_max3_f32 v190, v190, v105, v120
	v_max3_f32 v191, v191, v122, v123
	v_max3_f32 v190, v190, v121, v108
	v_max3_f32 v191, v191, v110, v111
	v_max3_f32 v190, v190, v109, v124
	v_mfma_f32_32x32x16_bf16 v[48:63], v[136:139], v[234:237], v[48:63]
	v_max3_f32 v191, v191, v126, v127
	v_max3_f32 v190, v190, v125, v191
	v_mov_b32_e32 v191, v190
	s_nop 1
	v_permlane32_swap_b32_e32 v190, v191
	v_mfma_f32_32x32x16_bf16 v[48:63], v[132:135], v[238:241], v[48:63]
	v_max_f32_e32 v234, v190, v191
	s_mov_b32 s2, 0x4138aa3b
	v_cmp_ge_f32_e32 vcc, s2, v234
	v_mfma_f32_32x32x16_bf16 v[48:63], v[128:131], v[242:245], v[48:63]
	s_cmp_eq_u64 vcc, exec
	v_mov_b32_e32 v202, 1.0
	s_cbranch_scc0 .LBB0_837

; #define SBAR() __builtin_amdgcn_sched_barrier(0)
; #define SLOAD(k0) do { vs0 = *reinterpret_cast<const bf16x8*>(&Vh[(size_t)((k0) + sr) * DM + sc]); vs1 = *reinterpret_cast<const bf16x8*>(&Vh[(size_t)((k0) + 32 + sr) * DM + sc]); \
;     ks = *reinterpret_cast<const bf16x8*>(&Kh[(size_t)((k0) + kr) * DM + kc]); } while (0)
; #define SWRITE(s) do { *(bf16x8*)(V_lds + (s) * SHM_V + vst0) = vs0; *(bf16x8*)(V_lds + (s) * SHM_V + vst1) = vs1; *(bf16x8*)(K_lds + (s) * SHM_K64 + kst) = ks; } while (0)
; #define RESC(a) do { if (__any((a) < 1.f)) { if (hi == 0) al_l[r32] = (a); asm volatile("s_waitcnt lgkmcnt(0)" ::: "memory"); \
;     _Pragma("unroll") for (int d = 0; d < 4; ++d) _Pragma("unroll") for (int r = 0; r < 16; ++r) o[d][r] *= al_l[crow(r, hi)]; } } while (0)
; #define ROT() do { s_prev = s_cur; s_cur = s_next; s_next = (s_next == DA_NBUF - 1) ? 0 : s_next + 1; } while (0)
; __device__ __forceinline__ void diff_pass(const bf16_t* __restrict__ Qb, const bf16_t* __restrict__ Kh, const bf16_t* __restrict__ Vh, int seq, char* lds, f32x16 (&o)[4], const int wave_) {
;     ...
;     for (int j = 1; j + 1 < NT; j += 2) {
;         SLOAD((j + 1) * 64);
;         SBAR(); qkt64c(pB0, pB1, K_lds + s_cur * SHM_K64, qr, negm, r32, hi); FIN(pA0, pA1, alA); SBAR();
;         YSEG(pB0, pB1, alB, s_prev);
;         SWRITE(s_next); RESC(alB); __syncthreads(); ROT();
;         SLOAD((j + 2) * 64);
;         SBAR(); qkt64c(pA0, pA1, K_lds + s_cur * SHM_K64, qr, negm, r32, hi); FIN(pB0, pB1, alB); SBAR();
;         YSEG(pA0, pA1, alA, s_prev);
;         SWRITE(s_next); RESC(alA); __syncthreads(); ROT();
.LBB0_834:
	s_add_i32 s2, s42, 1
	v_add_f32_e32 v128, v231, v232
	s_cmp_lg_u32 s42, 2
	v_fmac_f32_e32 v128, v215, v230
	v_add_f32_e32 v215, v203, v204
	s_cselect_b32 s2, s2, 0
	s_add_i32 s40, s40, 2
	s_mov_b64 s[8:9], 0x40000
	v_fmac_f32_e32 v215, v128, v233
	v_lshl_add_u64 v[198:199], v[198:199], 0, s[8:9]
	s_lshl_b32 s3, s42, 13
	s_cmp_gt_u32 s40, 28
	v_lshl_add_u64 v[200:201], v[200:201], 0, s[8:9]
	v_add_u32_e32 v128, s3, v223
	v_add_u32_e32 v129, s3, v226
	v_add_u32_e32 v130, s3, v228
	v_add_u32_e32 v131, s3, v229
	v_mov_b32_e32 v230, v202
	s_mov_b32 s12, s41
	s_mov_b32 s41, s2
	s_waitcnt lgkmcnt(0)
	s_barrier
	s_cbranch_scc1 .LBB0_838
	s_branch .Latt9_p1_top

; __device__ __forceinline__ void qkt64c(f32x16& p0, f32x16& p1, const char* Ks, const bf16x8* qr, const f32x16& cinit, int r32, int hi) {
; #pragma unroll
;     for (int d0 = 0; d0 < 4; ++d0) { const int cb = (d0 * 16 + hi * 8) * 2;
;         const bf16x8 b0 = *reinterpret_cast<const bf16x8*>(Ks + kswz<64>(r32, cb));
;         const bf16x8 b1 = *reinterpret_cast<const bf16x8*>(Ks + kswz<64>(32 + r32, cb));
;         if (d0 == 0) { p0 = __builtin_amdgcn_mfma_f32_32x32x16_bf16(b0, qr[0], cinit, 0, 0, 0); p1 = __builtin_amdgcn_mfma_f32_32x32x16_bf16(b1, qr[0], cinit, 0, 0, 0); }
;         else { p0 = __builtin_amdgcn_mfma_f32_32x32x16_bf16(b0, qr[d0], p0, 0, 0, 0); p1 = __builtin_amdgcn_mfma_f32_32x32x16_bf16(b1, qr[d0], p1, 0, 0, 0); } }
; }
.LBB0_846:
	s_lshl_b32 s2, s30, 13
	s_add_i32 s2, s2, 0
	v_add_u32_e32 v128, s2, v227
	v_add_u32_e32 v129, s2, v231
	v_add_u32_e32 v130, s2, v232
	v_add_u32_e32 v131, s2, v233
.Latt9_p2_top:
	ds_read_b128 v[144:147], v128 offset:49152
	ds_read_b128 v[148:151], v129 offset:49152
	ds_read_b128 v[152:155], v130 offset:49152
	ds_read_b128 v[156:159], v131 offset:49152
	ds_read_b128 v[190:193], v128 offset:53248
	ds_read_b128 v[236:239], v129 offset:53248
	ds_read_b128 v[240:243], v130 offset:53248
	ds_read_b128 v[244:247], v131 offset:53248
	v_lshl_add_u64 v[202:203], v[200:201], 0, s[64:65]
	s_mov_b32 s2, 0x8a40000
	v_add_co_u32_e32 v64, vcc, s2, v202
	s_mov_b32 s2, 0x8a50000
	s_nop 0
	v_addc_co_u32_e32 v65, vcc, 0, v203, vcc
	v_add_co_u32_e32 v66, vcc, s2, v202
	v_lshl_add_u64 v[204:205], v[198:199], 0, s[64:65]
	s_nop 0
	v_addc_co_u32_e32 v67, vcc, 0, v203, vcc
	s_mov_b32 s2, 0x6a40000
	global_load_dwordx4 v[178:181], v[64:65], off
	global_load_dwordx4 v[182:185], v[66:67], off
	v_add_co_u32_e32 v64, vcc, s2, v204
	s_nop 1
	v_addc_co_u32_e32 v65, vcc, 0, v205, vcc
	global_load_dwordx4 v[186:189], v[64:65], off offset:128
	v_exp_f32_e32 v208, v120
	v_exp_f32_e32 v209, v121
	v_add_f32_e32 v120, v96, v97
	v_add_f32_e32 v121, v98, v99
	s_waitcnt lgkmcnt(7)
	v_mfma_f32_32x32x16_bf16 v[128:143], v[144:147], v[162:165], v[80:95]
	v_exp_f32_e32 v210, v122
	v_add_f32_e32 v120, v120, v121
	v_add_f32_e32 v121, v100, v101
	v_add_f32_e32 v122, v102, v103
	v_exp_f32_e32 v211, v123
	s_waitcnt lgkmcnt(6)
	v_mfma_f32_32x32x16_bf16 v[128:143], v[148:151], v[166:169], v[128:143]
	v_add_f32_e32 v121, v121, v122
	v_add_f32_e32 v122, v104, v105
	v_add_f32_e32 v123, v106, v107
	v_add_f32_e32 v122, v122, v123
	v_add_f32_e32 v123, v108, v109
	s_waitcnt lgkmcnt(5)
	v_mfma_f32_32x32x16_bf16 v[128:143], v[152:155], v[170:173], v[128:143]
	v_exp_f32_e32 v124, v124
	v_exp_f32_e32 v125, v125
	v_exp_f32_e32 v126, v126
	v_exp_f32_e32 v127, v127
	v_cvt_pk_bf16_f32 v96, v96, v97
	s_waitcnt lgkmcnt(4)
	v_mfma_f32_32x32x16_bf16 v[128:143], v[156:159], v[174:177], v[128:143]
	v_cvt_pk_bf16_f32 v97, v98, v99
	v_cvt_pk_bf16_f32 v98, v100, v101
	v_cvt_pk_bf16_f32 v99, v102, v103
	s_nop 0
	v_permlane32_swap_b32_e32 v96, v98
	s_waitcnt lgkmcnt(3)
	v_mfma_f32_32x32x16_bf16 v[144:159], v[190:193], v[162:165], v[80:95]
	v_add_f32_e32 v190, v110, v111
	v_add_f32_e32 v123, v123, v190
	v_add_f32_e32 v190, v112, v113
	v_add_f32_e32 v191, v114, v115
	v_add_f32_e32 v190, v190, v191
	v_add_f32_e32 v120, v190, v120
	v_add_f32_e32 v190, v116, v117
	s_waitcnt lgkmcnt(2)
	v_mfma_f32_32x32x16_bf16 v[144:159], v[236:239], v[166:169], v[144:159]
	v_lshl_add_u32 v238, s12, 14, v221
	ds_read_b64_tr_b16 v[64:65], v238 offset:0
	ds_read_b64_tr_b16 v[66:67], v238 offset:0x800
	ds_read_b64_tr_b16 v[68:69], v238 offset:0x1000
	ds_read_b64_tr_b16 v[70:71], v238 offset:0x1800
	ds_read_b64_tr_b16 v[72:73], v238 offset:0x2000
	ds_read_b64_tr_b16 v[74:75], v238 offset:0x2800
	ds_read_b64_tr_b16 v[76:77], v238 offset:0x3000
	ds_read_b64_tr_b16 v[78:79], v238 offset:0x3800
	v_add_f32_e32 v191, v118, v119
	v_add_f32_e32 v190, v190, v191
	v_add_f32_e32 v121, v190, v121
	v_add_f32_e32 v190, v208, v209
	v_add_f32_e32 v191, v210, v211
	v_add_f32_e32 v190, v190, v191
	v_add_f32_e32 v122, v122, v190
	s_waitcnt lgkmcnt(9)
	v_mfma_f32_32x32x16_bf16 v[144:159], v[240:243], v[170:173], v[144:159]
	v_add_f32_e32 v190, v124, v125
	v_add_f32_e32 v191, v126, v127
	v_add_f32_e32 v190, v190, v191
	v_add_f32_e32 v123, v123, v190
	v_add_f32_e32 v120, v120, v121
	v_add_f32_e32 v121, v122, v123
	v_add_f32_e32 v235, v120, v121
	s_waitcnt lgkmcnt(8)
	v_mfma_f32_32x32x16_bf16 v[144:159], v[244:247], v[174:177], v[144:159]
	v_mov_b32_e32 v236, v235
	v_cvt_pk_bf16_f32 v120, v104, v105
	v_cvt_pk_bf16_f32 v121, v106, v107
	v_cvt_pk_bf16_f32 v122, v108, v109
	v_cvt_pk_bf16_f32 v123, v110, v111
	v_permlane32_swap_b32_e32 v97, v99
	v_cvt_pk_bf16_f32 v104, v112, v113
	v_cvt_pk_bf16_f32 v105, v114, v115
	v_cvt_pk_bf16_f32 v106, v116, v117
	v_cvt_pk_bf16_f32 v107, v118, v119
	s_waitcnt lgkmcnt(0)
	v_mfma_f32_32x32x16_bf16 v[0:15], v[96:99], v[64:67], v[0:15]
	v_permlane32_swap_b32_e32 v120, v122
	v_permlane32_swap_b32_e32 v121, v123
	v_cvt_pk_bf16_f32 v100, v208, v209
	v_cvt_pk_bf16_f32 v101, v210, v211
	v_cvt_pk_bf16_f32 v102, v124, v125
	v_cvt_pk_bf16_f32 v103, v126, v127
	v_mfma_f32_32x32x16_bf16 v[0:15], v[120:123], v[68:71], v[0:15]
	v_permlane32_swap_b32_e32 v104, v106
	v_permlane32_swap_b32_e32 v105, v107
	ds_read_b64_tr_b16 v[190:191], v238 offset:0x200
	ds_read_b64_tr_b16 v[192:193], v238 offset:0xa00
	ds_read_b64_tr_b16 v[240:241], v238 offset:0x1200
	ds_read_b64_tr_b16 v[242:243], v238 offset:0x1a00
	ds_read_b64_tr_b16 v[244:245], v238 offset:0x2200
	ds_read_b64_tr_b16 v[246:247], v238 offset:0x2a00
	ds_read_b64_tr_b16 v[208:209], v238 offset:0x3200
	ds_read_b64_tr_b16 v[210:211], v238 offset:0x3a00
	v_mfma_f32_32x32x16_bf16 v[0:15], v[104:107], v[72:75], v[0:15]
	v_permlane32_swap_b32_e32 v100, v102
	v_permlane32_swap_b32_e32 v101, v103
	v_permlane32_swap_b32_e32 v235, v236
	v_max_f32_e32 v108, v128, v129
	v_max3_f32 v108, v108, v144, v146
	v_max3_f32 v109, v130, v131, v145
	v_max3_f32 v108, v108, v147, v132
	v_max3_f32 v109, v109, v134, v135
	v_mfma_f32_32x32x16_bf16 v[0:15], v[100:103], v[76:79], v[0:15]
	v_max3_f32 v237, v108, v133, v148
	v_max3_f32 v239, v109, v150, v151
	ds_read_b64_tr_b16 v[124:125], v238 offset:0x400
	ds_read_b64_tr_b16 v[126:127], v238 offset:0xc00
	ds_read_b64_tr_b16 v[116:117], v238 offset:0x1400
	ds_read_b64_tr_b16 v[118:119], v238 offset:0x1c00
	ds_read_b64_tr_b16 v[112:113], v238 offset:0x2400
	ds_read_b64_tr_b16 v[114:115], v238 offset:0x2c00
	ds_read_b64_tr_b16 v[108:109], v238 offset:0x3400
	ds_read_b64_tr_b16 v[110:111], v238 offset:0x3c00
	s_waitcnt lgkmcnt(8)
	v_mfma_f32_32x32x16_bf16 v[48:63], v[96:99], v[190:193], v[48:63]
	v_max3_f32 v190, v237, v149, v136
	v_max3_f32 v191, v239, v138, v139
	v_max3_f32 v190, v190, v137, v152
	v_max3_f32 v191, v191, v154, v155
	v_max3_f32 v190, v190, v153, v140
	v_max3_f32 v191, v191, v142, v143
	v_max3_f32 v190, v190, v141, v156
	v_mfma_f32_32x32x16_bf16 v[48:63], v[120:123], v[240:243], v[48:63]
	v_max3_f32 v191, v191, v158, v159
	v_max3_f32 v190, v190, v157, v191
	v_mov_b32_e32 v191, v190
	s_nop 1
	v_permlane32_swap_b32_e32 v190, v191
	v_mfma_f32_32x32x16_bf16 v[48:63], v[104:107], v[244:247], v[48:63]
	v_max_f32_e32 v237, v190, v191
	s_mov_b32 s2, 0x4138aa3b
	v_cmp_ge_f32_e32 vcc, s2, v237
	v_mfma_f32_32x32x16_bf16 v[48:63], v[100:103], v[208:211], v[48:63]
	s_cmp_eq_u64 vcc, exec
	s_cbranch_scc0 .LBB0_859
	v_mov_b32_e32 v237, 1.0

; __device__ __forceinline__ void qkt64c(f32x16& p0, f32x16& p1, const char* Ks, const bf16x8* qr, const f32x16& cinit, int r32, int hi) {
; #pragma unroll
;     for (int d0 = 0; d0 < 4; ++d0) { const int cb = (d0 * 16 + hi * 8) * 2;
;         const bf16x8 b0 = *reinterpret_cast<const bf16x8*>(Ks + kswz<64>(r32, cb));
;         const bf16x8 b1 = *reinterpret_cast<const bf16x8*>(Ks + kswz<64>(32 + r32, cb));
;         if (d0 == 0) { p0 = __builtin_amdgcn_mfma_f32_32x32x16_bf16(b0, qr[0], cinit, 0, 0, 0); p1 = __builtin_amdgcn_mfma_f32_32x32x16_bf16(b1, qr[0], cinit, 0, 0, 0); }
;         else { p0 = __builtin_amdgcn_mfma_f32_32x32x16_bf16(b0, qr[d0], p0, 0, 0, 0); p1 = __builtin_amdgcn_mfma_f32_32x32x16_bf16(b1, qr[d0], p1, 0, 0, 0); } }
; }
.LBB0_852:
	v_add_co_u32_e32 v96, vcc, 0x8a60000, v202
	s_waitcnt lgkmcnt(0)
	s_nop 0
	v_addc_co_u32_e32 v97, vcc, 0, v203, vcc
	v_add_co_u32_e32 v98, vcc, 0x8a70000, v202
	s_nop 1
	v_addc_co_u32_e32 v99, vcc, 0, v203, vcc
	v_add_co_u32_e32 v100, vcc, 0x6a60000, v204
	s_nop 1
	v_addc_co_u32_e32 v101, vcc, 0, v205, vcc
	v_add_u32_e32 v102, s2, v227
	v_add_u32_e32 v103, s2, v231
	v_add_u32_e32 v104, s2, v232
	v_add_u32_e32 v105, s2, v233
	s_barrier
	ds_read_b128 v[112:115], v102 offset:49152
	ds_read_b128 v[116:119], v103 offset:49152
	ds_read_b128 v[120:123], v104 offset:49152
	ds_read_b128 v[124:127], v105 offset:49152
	ds_read_b128 v[190:193], v102 offset:53248
	ds_read_b128 v[202:205], v103 offset:53248
	ds_read_b128 v[208:211], v104 offset:53248
	ds_read_b128 v[238:241], v105 offset:53248
	global_load_dwordx4 v[178:181], v[96:97], off
	global_load_dwordx4 v[182:185], v[98:99], off
	global_load_dwordx4 v[186:189], v[100:101], off offset:128
	v_exp_f32_e32 v242, v152
	v_exp_f32_e32 v243, v153
	v_add_f32_e32 v152, v128, v129
	v_add_f32_e32 v153, v130, v131
	s_waitcnt lgkmcnt(7)
	v_mfma_f32_32x32x16_bf16 v[96:111], v[112:115], v[162:165], v[80:95]
	v_exp_f32_e32 v244, v154
	v_add_f32_e32 v152, v152, v153
	v_add_f32_e32 v153, v132, v133
	v_add_f32_e32 v154, v134, v135
	v_exp_f32_e32 v245, v155
	s_waitcnt lgkmcnt(6)
	v_mfma_f32_32x32x16_bf16 v[96:111], v[116:119], v[166:169], v[96:111]
	v_add_f32_e32 v153, v153, v154
	v_add_f32_e32 v154, v136, v137
	v_add_f32_e32 v155, v138, v139
	v_add_f32_e32 v154, v154, v155
	v_add_f32_e32 v155, v140, v141
	s_waitcnt lgkmcnt(5)
	v_mfma_f32_32x32x16_bf16 v[96:111], v[120:123], v[170:173], v[96:111]
	v_exp_f32_e32 v156, v156
	v_exp_f32_e32 v157, v157
	v_exp_f32_e32 v158, v158
	v_exp_f32_e32 v159, v159
	s_waitcnt lgkmcnt(4)
	v_mfma_f32_32x32x16_bf16 v[96:111], v[124:127], v[174:177], v[96:111]
	s_waitcnt lgkmcnt(3)
	v_mfma_f32_32x32x16_bf16 v[112:127], v[190:193], v[162:165], v[80:95]
	v_add_f32_e32 v190, v142, v143
	v_add_f32_e32 v155, v155, v190
	v_add_f32_e32 v190, v144, v145
	v_add_f32_e32 v191, v146, v147
	v_add_f32_e32 v190, v190, v191
	v_add_f32_e32 v152, v152, v190
	v_add_f32_e32 v190, v148, v149
	s_waitcnt lgkmcnt(2)
	v_mfma_f32_32x32x16_bf16 v[112:127], v[202:205], v[166:169], v[112:127]
	v_lshl_add_u32 v205, s30, 14, v221
	ds_read_b64_tr_b16 v[64:65], v205 offset:0
	ds_read_b64_tr_b16 v[66:67], v205 offset:0x800
	ds_read_b64_tr_b16 v[68:69], v205 offset:0x1000
	ds_read_b64_tr_b16 v[70:71], v205 offset:0x1800
	ds_read_b64_tr_b16 v[72:73], v205 offset:0x2000
	ds_read_b64_tr_b16 v[74:75], v205 offset:0x2800
	ds_read_b64_tr_b16 v[76:77], v205 offset:0x3000
	ds_read_b64_tr_b16 v[78:79], v205 offset:0x3800
	v_add_f32_e32 v191, v150, v151
	v_add_f32_e32 v190, v190, v191
	v_add_f32_e32 v153, v153, v190
	v_add_f32_e32 v190, v242, v243
	v_add_f32_e32 v191, v244, v245
	v_add_f32_e32 v190, v190, v191
	v_add_f32_e32 v154, v154, v190
	s_waitcnt lgkmcnt(9)
	v_mfma_f32_32x32x16_bf16 v[112:127], v[208:211], v[170:173], v[112:127]
	v_add_f32_e32 v190, v156, v157
	v_add_f32_e32 v191, v158, v159
	v_add_f32_e32 v190, v190, v191
	v_add_f32_e32 v155, v155, v190
	v_add_f32_e32 v152, v152, v153
	v_add_f32_e32 v153, v154, v155
	v_add_f32_e32 v203, v152, v153
	s_waitcnt lgkmcnt(8)
	v_mfma_f32_32x32x16_bf16 v[112:127], v[238:241], v[174:177], v[112:127]
	v_mov_b32_e32 v204, v203
	v_cvt_pk_bf16_f32 v152, v128, v129
	v_cvt_pk_bf16_f32 v153, v130, v131
	v_cvt_pk_bf16_f32 v154, v132, v133
	v_cvt_pk_bf16_f32 v155, v134, v135
	v_cvt_pk_bf16_f32 v136, v136, v137
	v_cvt_pk_bf16_f32 v137, v138, v139
	v_cvt_pk_bf16_f32 v138, v140, v141
	v_cvt_pk_bf16_f32 v139, v142, v143
	v_permlane32_swap_b32_e32 v152, v154
	v_permlane32_swap_b32_e32 v153, v155
	v_cvt_pk_bf16_f32 v132, v144, v145
	v_cvt_pk_bf16_f32 v133, v146, v147
	v_cvt_pk_bf16_f32 v134, v148, v149
	v_cvt_pk_bf16_f32 v135, v150, v151
	s_waitcnt lgkmcnt(0)
	v_mfma_f32_32x32x16_bf16 v[0:15], v[152:155], v[64:67], v[0:15]
	v_permlane32_swap_b32_e32 v136, v138
	v_permlane32_swap_b32_e32 v137, v139
	v_cvt_pk_bf16_f32 v128, v242, v243
	v_cvt_pk_bf16_f32 v129, v244, v245
	v_cvt_pk_bf16_f32 v130, v156, v157
	v_cvt_pk_bf16_f32 v131, v158, v159
	v_mfma_f32_32x32x16_bf16 v[0:15], v[136:139], v[68:71], v[0:15]
	v_permlane32_swap_b32_e32 v132, v134
	v_permlane32_swap_b32_e32 v133, v135
	ds_read_b64_tr_b16 v[190:191], v205 offset:0x200
	ds_read_b64_tr_b16 v[192:193], v205 offset:0xa00
	ds_read_b64_tr_b16 v[208:209], v205 offset:0x1200
	ds_read_b64_tr_b16 v[210:211], v205 offset:0x1a00
	ds_read_b64_tr_b16 v[238:239], v205 offset:0x2200
	ds_read_b64_tr_b16 v[240:241], v205 offset:0x2a00
	ds_read_b64_tr_b16 v[242:243], v205 offset:0x3200
	ds_read_b64_tr_b16 v[244:245], v205 offset:0x3a00
	v_mfma_f32_32x32x16_bf16 v[0:15], v[132:135], v[72:75], v[0:15]
	v_permlane32_swap_b32_e32 v128, v130
	v_permlane32_swap_b32_e32 v129, v131
	v_permlane32_swap_b32_e32 v203, v204
	v_max_f32_e32 v140, v96, v97
	v_max3_f32 v140, v140, v112, v114
	v_max3_f32 v141, v98, v99, v113
	v_max3_f32 v140, v140, v115, v100
	v_max3_f32 v141, v141, v102, v103
	v_mfma_f32_32x32x16_bf16 v[0:15], v[128:131], v[76:79], v[0:15]
	v_max3_f32 v202, v140, v101, v116
	v_max3_f32 v246, v141, v118, v119
	ds_read_b64_tr_b16 v[156:157], v205 offset:0x400
	ds_read_b64_tr_b16 v[158:159], v205 offset:0xc00
	ds_read_b64_tr_b16 v[148:149], v205 offset:0x1400
	ds_read_b64_tr_b16 v[150:151], v205 offset:0x1c00
	ds_read_b64_tr_b16 v[144:145], v205 offset:0x2400
	ds_read_b64_tr_b16 v[146:147], v205 offset:0x2c00
	ds_read_b64_tr_b16 v[140:141], v205 offset:0x3400
	ds_read_b64_tr_b16 v[142:143], v205 offset:0x3c00
	s_waitcnt lgkmcnt(8)
	v_mfma_f32_32x32x16_bf16 v[48:63], v[152:155], v[190:193], v[48:63]
	v_max3_f32 v190, v202, v117, v104
	v_max3_f32 v191, v246, v106, v107
	v_max3_f32 v190, v190, v105, v120
	v_max3_f32 v191, v191, v122, v123
	v_max3_f32 v190, v190, v121, v108
	v_max3_f32 v191, v191, v110, v111
	v_max3_f32 v190, v190, v109, v124
	v_mfma_f32_32x32x16_bf16 v[48:63], v[136:139], v[208:211], v[48:63]
	v_max3_f32 v191, v191, v126, v127
	v_max3_f32 v190, v190, v125, v191
	v_mov_b32_e32 v191, v190
	s_nop 1
	v_permlane32_swap_b32_e32 v190, v191
	v_mfma_f32_32x32x16_bf16 v[48:63], v[132:135], v[238:241], v[48:63]
	v_max_f32_e32 v238, v190, v191
	s_mov_b32 s2, 0x4138aa3b
	v_cmp_ge_f32_e32 vcc, s2, v238
	v_mfma_f32_32x32x16_bf16 v[48:63], v[128:131], v[242:245], v[48:63]
	s_cmp_eq_u64 vcc, exec
	v_mov_b32_e32 v202, 1.0
	s_cbranch_scc0 .LBB0_860

; #define SBAR() __builtin_amdgcn_sched_barrier(0)
; #define SLOAD(k0) do { vs0 = *reinterpret_cast<const bf16x8*>(&Vh[(size_t)((k0) + sr) * DM + sc]); vs1 = *reinterpret_cast<const bf16x8*>(&Vh[(size_t)((k0) + 32 + sr) * DM + sc]); \
;     ks = *reinterpret_cast<const bf16x8*>(&Kh[(size_t)((k0) + kr) * DM + kc]); } while (0)
; #define SWRITE(s) do { *(bf16x8*)(V_lds + (s) * SHM_V + vst0) = vs0; *(bf16x8*)(V_lds + (s) * SHM_V + vst1) = vs1; *(bf16x8*)(K_lds + (s) * SHM_K64 + kst) = ks; } while (0)
; #define RESC(a) do { if (__any((a) < 1.f)) { if (hi == 0) al_l[r32] = (a); asm volatile("s_waitcnt lgkmcnt(0)" ::: "memory"); \
;     _Pragma("unroll") for (int d = 0; d < 4; ++d) _Pragma("unroll") for (int r = 0; r < 16; ++r) o[d][r] *= al_l[crow(r, hi)]; } } while (0)
; #define ROT() do { s_prev = s_cur; s_cur = s_next; s_next = (s_next == DA_NBUF - 1) ? 0 : s_next + 1; } while (0)
; __device__ __forceinline__ void diff_pass(const bf16_t* __restrict__ Qb, const bf16_t* __restrict__ Kh, const bf16_t* __restrict__ Vh, int seq, char* lds, f32x16 (&o)[4], const int wave_) {
;     ...
;     for (int j = 1; j + 1 < NT; j += 2) {
;         SLOAD((j + 1) * 64);
;         SBAR(); qkt64c(pB0, pB1, K_lds + s_cur * SHM_K64, qr, negm, r32, hi); FIN(pA0, pA1, alA); SBAR();
;         YSEG(pB0, pB1, alB, s_prev);
;         SWRITE(s_next); RESC(alB); __syncthreads(); ROT();
;         SLOAD((j + 2) * 64);
;         SBAR(); qkt64c(pA0, pA1, K_lds + s_cur * SHM_K64, qr, negm, r32, hi); FIN(pB0, pB1, alB); SBAR();
;         YSEG(pA0, pA1, alA, s_prev);
;         SWRITE(s_next); RESC(alA); __syncthreads(); ROT();
.LBB0_857:
	s_add_i32 s2, s30, 1
	v_add_f32_e32 v128, v235, v236
	s_cmp_lg_u32 s30, 2
	v_fmac_f32_e32 v128, v219, v234
	v_add_f32_e32 v219, v203, v204
	s_cselect_b32 s2, s2, 0
	s_add_i32 s28, s28, 2
	s_mov_b64 s[8:9], 0x40000
	v_fmac_f32_e32 v219, v128, v237
	v_lshl_add_u64 v[198:199], v[198:199], 0, s[8:9]
	s_lshl_b32 s3, s30, 13
	s_cmp_gt_u32 s28, 28
	v_lshl_add_u64 v[200:201], v[200:201], 0, s[8:9]
	v_add_u32_e32 v128, s3, v227
	v_add_u32_e32 v129, s3, v231
	v_add_u32_e32 v130, s3, v232
	v_add_u32_e32 v131, s3, v233
	v_mov_b32_e32 v234, v202
	s_mov_b32 s12, s29
	s_mov_b32 s29, s2
	s_waitcnt lgkmcnt(0)
	s_barrier
	s_cbranch_scc1 .LBB0_861
	s_branch .Latt9_p2_top
